# speedup vs baseline: 1.0231x; 1.0048x over previous
_Z8k_layer2PK15HIP_vector_typeIfLj2EES2_PKiS4_PS0_:
	s_lshl_b32 s3, s2, 7
	s_and_b32 s3, s3, 0x380
	s_lshr_b32 s2, s2, 3
	s_add_i32 s2, s3, s2
	s_mul_i32 s3, s2, 0x62
	v_lshrrev_b32_e32 v1, 2, v0
	s_cmpk_lt_u32 s2, 0x3fd
	s_movk_i32 s2, 0x188
	s_load_dwordx4 s[4:7], s[0:1], 0x8
	s_load_dwordx2 s[16:17], s[0:1], 0x0
	s_load_dwordx2 s[18:19], s[0:1], 0x18
	s_load_dwordx2 s[20:21], s[0:1], 0x20
	v_add_u32_e32 v1, s3, v1
	s_cselect_b64 s[8:9], -1, 0
	v_cmp_gt_u32_e32 vcc, s2, v0
	s_mov_b32 s2, 0x186a0
	v_cmp_gt_i32_e64 s[2:3], s2, v1
	s_and_b64 s[8:9], s[8:9], vcc
	v_ashrrev_i32_e32 v2, 31, v1
	s_and_b64 vcc, s[8:9], s[2:3]
	v_cndmask_b32_e32 v3, 0, v2, vcc
	v_mov_b32_e32 v2, 0x1869f
	v_cndmask_b32_e32 v2, v2, v1, vcc
	s_waitcnt lgkmcnt(0)
	v_lshl_add_u64 v[4:5], v[2:3], 2, s[6:7]
	global_load_dword v12, v[4:5], off
	v_mov_b32_e32 v7, 0
	v_mov_b32_e32 v24, 0
	s_and_saveexec_b64 s[2:3], vcc
	s_cbranch_execz .LBB2_2
	global_load_dword v1, v[4:5], off offset:4
	s_waitcnt vmcnt(0)
	v_sub_u32_e32 v24, v1, v12
.LBB2_2:
	s_or_b64 exec, exec, s[2:3]
	v_lshl_add_u64 v[4:5], v[2:3], 3, s[4:5]
	global_load_dwordx2 v[4:5], v[4:5], off
	s_mov_b64 s[4:5], s[20:21]
	v_and_b32_e32 v0, 3, v0
	s_mov_b32 s14, 0
	v_cmp_lt_i32_e64 s[2:3], 0, v24
	v_mov_b32_e32 v6, 0
	s_and_saveexec_b64 s[6:7], s[2:3]
	s_cbranch_execz .LBB2_22
	s_mov_b64 s[2:3], s[16:17]
	s_mov_b64 s[8:9], s[18:19]
	v_mov_b32_e32 v9, 0
	s_waitcnt vmcnt(1)
	v_ashrrev_i32_e32 v13, 31, v12
	v_mov_b32_e32 v1, v9
	v_lshl_add_u64 v[6:7], v[12:13], 0, v[0:1]
	s_waitcnt lgkmcnt(0)
	v_lshl_add_u64 v[6:7], v[6:7], 2, s[8:9]
	v_lshl_add_u64 v[10:11], v[6:7], 0, 32
	v_add_u32_e32 v1, v12, v0
	s_mov_b64 s[10:11], 0
	v_mov_b32_e32 v6, v9
	v_mov_b32_e32 v7, v9
	s_branch .LBB2_5

	.amdhsa_kernel _Z8k_layer2PK15HIP_vector_typeIfLj2EES2_PKiS4_PS0_
		.amdhsa_group_segment_fixed_size 0
		.amdhsa_private_segment_fixed_size 0
		.amdhsa_kernarg_size 40
		.amdhsa_user_sgpr_count 2
		.amdhsa_user_sgpr_dispatch_ptr 0
		.amdhsa_user_sgpr_queue_ptr 0
		.amdhsa_user_sgpr_kernarg_segment_ptr 1
		.amdhsa_user_sgpr_dispatch_id 0
		.amdhsa_user_sgpr_kernarg_preload_length 0
		.amdhsa_user_sgpr_kernarg_preload_offset 0
		.amdhsa_user_sgpr_private_segment_size 0
		.amdhsa_uses_dynamic_stack 0
		.amdhsa_enable_private_segment 0
		.amdhsa_system_sgpr_workgroup_id_x 1
		.amdhsa_system_sgpr_workgroup_id_y 0
		.amdhsa_system_sgpr_workgroup_id_z 0
		.amdhsa_system_sgpr_workgroup_info 0
		.amdhsa_system_vgpr_workitem_id 0
		.amdhsa_next_free_vgpr 25
		.amdhsa_next_free_sgpr 22
		.amdhsa_accum_offset 28
		.amdhsa_reserve_vcc 1
		.amdhsa_float_round_mode_32 0
		.amdhsa_float_round_mode_16_64 0
		.amdhsa_float_denorm_mode_32 3
		.amdhsa_float_denorm_mode_16_64 3
		.amdhsa_dx10_clamp 1
		.amdhsa_ieee_mode 1
		.amdhsa_fp16_overflow 0
		.amdhsa_tg_split 0
		.amdhsa_exception_fp_ieee_invalid_op 0
		.amdhsa_exception_fp_denorm_src 0
		.amdhsa_exception_fp_ieee_div_zero 0
		.amdhsa_exception_fp_ieee_overflow 0
		.amdhsa_exception_fp_ieee_underflow 0
		.amdhsa_exception_fp_ieee_inexact 0
		.amdhsa_exception_int_div_zero 0
	.end_amdhsa_kernel

amdhsa.kernels:
  - .agpr_count:     0
    .args:
      - .actual_access:  read_only
        .address_space:  global
        .offset:         0
        .size:           8
        .value_kind:     global_buffer
      - .actual_access:  read_only
        .address_space:  global
        .offset:         8
        .size:           8
        .value_kind:     global_buffer
      - .actual_access:  read_only
        .address_space:  global
        .offset:         16
        .size:           8
        .value_kind:     global_buffer
      - .actual_access:  read_only
        .address_space:  global
        .offset:         24
        .size:           8
        .value_kind:     global_buffer
      - .actual_access:  read_only
        .address_space:  global
        .offset:         32
        .size:           8
        .value_kind:     global_buffer
      - .actual_access:  read_only
        .address_space:  global
        .offset:         40
        .size:           8
        .value_kind:     global_buffer
      - .actual_access:  write_only
        .address_space:  global
        .offset:         48
        .size:           8
        .value_kind:     global_buffer
      - .actual_access:  write_only
        .address_space:  global
        .offset:         56
        .size:           8
        .value_kind:     global_buffer
      - .actual_access:  write_only
        .address_space:  global
        .offset:         64
        .size:           8
        .value_kind:     global_buffer
      - .actual_access:  write_only
        .address_space:  global
        .offset:         72
        .size:           8
        .value_kind:     global_buffer
      - .actual_access:  write_only
        .address_space:  global
        .offset:         80
        .size:           8
        .value_kind:     global_buffer
    .group_segment_fixed_size: 20544
    .kernarg_segment_align: 8
    .kernarg_segment_size: 88
    .language:       OpenCL C
    .language_version:
      - 2
      - 0
    .max_flat_workgroup_size: 1024
    .name:           _Z6k_partPKiPKfS2_S2_S2_S2_PiS3_PDF16_S4_S4_
    .private_segment_fixed_size: 0
    .sgpr_count:     28
    .sgpr_spill_count: 0
    .symbol:         _Z6k_partPKiPKfS2_S2_S2_S2_PiS3_PDF16_S4_S4_.kd
    .uniform_work_group_size: 1
    .uses_dynamic_stack: false
    .vgpr_count:     44
    .vgpr_spill_count: 0
    .wavefront_size: 64
  - .agpr_count:     0
    .args:
      - .actual_access:  read_only
        .address_space:  global
        .offset:         0
        .size:           8
        .value_kind:     global_buffer
      - .actual_access:  read_only
        .address_space:  global
        .offset:         8
        .size:           8
        .value_kind:     global_buffer
      - .actual_access:  read_only
        .address_space:  global
        .offset:         16
        .size:           8
        .value_kind:     global_buffer
      - .actual_access:  write_only
        .address_space:  global
        .offset:         24
        .size:           8
        .value_kind:     global_buffer
      - .address_space:  global
        .offset:         32
        .size:           8
        .value_kind:     global_buffer
      - .actual_access:  read_only
        .address_space:  global
        .offset:         40
        .size:           8
        .value_kind:     global_buffer
      - .actual_access:  read_only
        .address_space:  global
        .offset:         48
        .size:           8
        .value_kind:     global_buffer
      - .actual_access:  read_only
        .address_space:  global
        .offset:         56
        .size:           8
        .value_kind:     global_buffer
      - .actual_access:  read_only
        .address_space:  global
        .offset:         64
        .size:           8
        .value_kind:     global_buffer
      - .actual_access:  write_only
        .address_space:  global
        .offset:         72
        .size:           8
        .value_kind:     global_buffer
      - .actual_access:  write_only
        .address_space:  global
        .offset:         80
        .size:           8
        .value_kind:     global_buffer
    .group_segment_fixed_size: 38832
    .kernarg_segment_align: 8
    .kernarg_segment_size: 88
    .language:       OpenCL C
    .language_version:
      - 2
      - 0
    .max_flat_workgroup_size: 512
    .name:           _Z8k_layer1PKDF16_PKiS2_PiS3_PKDv4_jS6_PKfS8_P15HIP_vector_typeIfLj2EESB_
    .private_segment_fixed_size: 0
    .sgpr_count:     76
    .sgpr_spill_count: 0
    .symbol:         _Z8k_layer1PKDF16_PKiS2_PiS3_PKDv4_jS6_PKfS8_P15HIP_vector_typeIfLj2EESB_.kd
    .uniform_work_group_size: 1
    .uses_dynamic_stack: false
    .vgpr_count:     64
    .vgpr_spill_count: 0
    .wavefront_size: 64
  - .agpr_count:     0
    .args:
      - .actual_access:  read_only
        .address_space:  global
        .offset:         0
        .size:           8
        .value_kind:     global_buffer
      - .actual_access:  read_only
        .address_space:  global
        .offset:         8
        .size:           8
        .value_kind:     global_buffer
      - .actual_access:  read_only
        .address_space:  global
        .offset:         16
        .size:           8
        .value_kind:     global_buffer
      - .actual_access:  read_only
        .address_space:  global
        .offset:         24
        .size:           8
        .value_kind:     global_buffer
      - .actual_access:  write_only
        .address_space:  global
        .offset:         32
        .size:           8
        .value_kind:     global_buffer
    .group_segment_fixed_size: 0
    .kernarg_segment_align: 8
    .kernarg_segment_size: 40
    .language:       OpenCL C
    .language_version:
      - 2
      - 0
    .max_flat_workgroup_size: 448
    .name:           _Z8k_layer2PK15HIP_vector_typeIfLj2EES2_PKiS4_PS0_
    .private_segment_fixed_size: 0
    .sgpr_count:     28
    .sgpr_spill_count: 0
    .symbol:         _Z8k_layer2PK15HIP_vector_typeIfLj2EES2_PKiS4_PS0_.kd
    .uniform_work_group_size: 1
    .uses_dynamic_stack: false
    .vgpr_count:     25
    .vgpr_spill_count: 0
    .wavefront_size: 64
